# phase 7 tail (out-proj / query weight rows -> int8): each wave's rows for both loops fetched at the start of the phase into free registers; plus phase-3 next-row prefetch
# baseline (speedup 1.0000x reference)
; __device__ void phase_ssm_post(KParams& p, int bid, int nb, char* smem) {
;   const int lane = threadIdx.x & 63, w = threadIdx.x >> 6;
;   for (int t = bid * 4 + w; t < T; t += nb * 4) {
;     ...
;   quant_weight_rows_i8(p.w_out_t, p.wo8, p.woscale, D, bid, nb);
;   quant_weight_rows_i8(p.w_q_t, p.wq8, p.wqscale, 1024, bid, nb);
.Lgb_wd_6:
.LBB0_1000:
	s_or_b64 exec, exec, s[6:7]
	s_movk_i32 s6, 0x2000
	v_mov_b32_e32 v191, 0
	s_mov_b64 s[16:17], s[0:1]
	s_load_dwordx4 s[60:63], s[16:17], 0x150
	v_cmp_gt_i32_e64 s[6:7], s6, v186
	v_lshlrev_b32_e32 v134, 2, v190
	s_waitcnt lgkmcnt(0)
	s_barrier
	v_lshlrev_b64 v[132:133], 12, v[186:187]
	v_or_b32_e32 v132, v132, v188
	v_lshl_add_u64 v[136:137], s[60:61], 0, v[132:133]
	global_load_dwordx4 v[100:103], v[136:137], off
	global_load_dwordx4 v[104:107], v[136:137], off offset:1024
	global_load_dwordx4 v[108:111], v[136:137], off offset:2048
	global_load_dwordx4 v[112:115], v[136:137], off offset:3072
	v_lshl_add_u64 v[138:139], s[62:63], 0, v[132:133]
	global_load_dwordx4 v[116:119], v[138:139], off
	global_load_dwordx4 v[120:123], v[138:139], off offset:1024
	global_load_dwordx4 v[124:127], v[138:139], off offset:2048
	global_load_dwordx4 v[128:131], v[138:139], off offset:3072
	s_and_saveexec_b64 s[18:19], s[6:7]
	s_cbranch_execz .LBB0_1005
	v_cmp_lt_i32_e32 vcc, v179, v180
	s_load_dwordx4 s[12:15], s[16:17], 0x90
	s_load_dwordx2 s[22:23], s[16:17], 0xa0
	v_cndmask_b32_e32 v2, v178, v179, vcc
	v_cmp_lt_i32_e32 vcc, v181, v180
	s_load_dwordx4 s[24:27], s[16:17], 0x208
	s_load_dwordx2 s[28:29], s[16:17], 0x228
	s_load_dwordx2 s[30:31], s[16:17], 0x1f0
	s_load_dwordx2 s[36:37], s[16:17], 0x1a8
	s_load_dwordx2 s[38:39], s[16:17], 0x118
	s_load_dwordx2 s[40:41], s[16:17], 0x128
	v_lshlrev_b32_e32 v39, 2, v2
	v_cndmask_b32_e32 v2, v178, v181, vcc
	v_or_b32_e32 v6, 0x100, v190
	v_or_b32_e32 v10, 0x200, v190
	v_or_b32_e32 v14, 0x300, v190
	v_lshlrev_b32_e32 v74, 2, v2
	v_lshrrev_b32_e32 v2, 2, v184
	v_lshrrev_b32_e32 v6, 4, v6
	v_lshrrev_b32_e32 v10, 4, v10
	v_lshrrev_b32_e32 v14, 4, v14
	s_lshl_b32 s20, s34, 2
	v_and_b32_e32 v4, 12, v2
	v_mov_b32_e32 v5, v191
	v_and_b32_e32 v8, 28, v6
	v_mov_b32_e32 v9, v191
	v_and_b32_e32 v12, 44, v10
	v_mov_b32_e32 v13, v191
	v_and_b32_e32 v16, 60, v14
	v_mov_b32_e32 v17, v191
	s_waitcnt lgkmcnt(0)
	v_lshl_add_u64 v[2:3], s[12:13], 0, v[4:5]
	v_lshl_add_u64 v[6:7], s[12:13], 0, v[8:9]
	v_lshl_add_u64 v[10:11], s[12:13], 0, v[12:13]
	v_lshl_add_u64 v[14:15], s[12:13], 0, v[16:17]
	v_mov_b32_e32 v135, v191
	v_lshlrev_b32_e32 v24, 1, v190
	v_mov_b32_e32 v25, v191
	s_ashr_i32 s21, s20, 31
	v_lshlrev_b64 v[34:35], 12, v[186:187]
	s_movk_i32 s12, 0xc00
	v_mov_b64_e32 v[36:37], s[30:31]
	v_lshl_add_u64 v[4:5], s[14:15], 0, v[4:5]
	v_lshl_add_u64 v[8:9], s[14:15], 0, v[8:9]
	v_lshl_add_u64 v[12:13], s[14:15], 0, v[12:13]
	v_lshl_add_u64 v[16:17], s[14:15], 0, v[16:17]
	v_lshl_add_u64 v[18:19], s[22:23], 0, v[134:135]
	v_lshl_add_u64 v[20:21], s[24:25], 0, v[24:25]
	v_lshl_add_u64 v[22:23], s[26:27], 0, v[24:25]
	v_lshl_add_u64 v[24:25], s[36:37], 0, v[24:25]
	v_lshl_add_u64 v[26:27], s[38:39], 0, v[190:191]
	v_lshl_add_u64 v[28:29], v[186:187], 2, s[40:41]
	s_lshl_b64 s[14:15], s[20:21], 2
	v_lshlrev_b64 v[30:31], 11, v[186:187]
	s_lshl_b64 s[22:23], s[20:21], 11
	v_lshlrev_b32_e32 v32, 3, v184
	v_mov_b32_e32 v33, v191
	v_lshl_add_u64 v[34:35], s[28:29], 0, v[34:35]
	s_lshl_b64 s[24:25], s[20:21], 12
	v_mad_i64_i32 v[36:37], s[12:13], v186, s12, v[36:37]
	s_mul_i32 s26, s34, 0x3000
	s_mul_hi_i32 s27, s20, 0xc00
	s_mov_b64 s[28:29], 0
	s_mov_b32 s30, 0x3b000000
	v_mov_b32_e32 v38, 0x358637bd
	s_mov_b32 s21, 0x800000
	s_mov_b32 s31, 0x42fe0000
	s_mov_b32 s36, 0xc0c0500
	s_mov_b32 s37, 0x40c0c00
	s_movk_i32 s38, 0x1fff
	v_mov_b32_e32 v75, v186
	s_branch .LBB0_1003

; __device__ __forceinline__ void quant_weight_rows_i8(const bf16_t* __restrict__ src, int8_t* __restrict__ dst, float* __restrict__ scl,
;                                                      int nrows, int bid, int nb) {
;   const int lane = threadIdx.x & 63, w = threadIdx.x >> 6;
;   for (int n = bid * 4 + w; n < nrows; n += nb * 4) {
;     const bf16_t* wr = src + (size_t)n * D;
;     uint4 q[4];
; #pragma unroll
;     for (int c = 0; c < 4; ++c) q[c] = *reinterpret_cast<const uint4*>(wr + c * 512 + lane * 8);
; __device__ void phase_ssm_post(KParams& p, int bid, int nb, char* smem) {
;     ...
;   quant_weight_rows_i8(p.w_out_t, p.wo8, p.woscale, D, bid, nb);
.LBB0_1005:
	s_or_b64 exec, exec, s[18:19]
	s_movk_i32 s12, 0x800
	v_cmp_gt_i32_e32 vcc, s12, v186
	s_and_saveexec_b64 s[12:13], vcc
	s_cbranch_execz .LBB0_1010
	s_load_dwordx2 s[22:23], s[16:17], 0x120
	s_load_dwordx2 s[18:19], s[16:17], 0x130
	s_load_dwordx2 s[20:21], s[16:17], 0x150
	v_cmp_lt_i32_e32 vcc, v179, v180
	v_lshlrev_b64 v[4:5], 12, v[186:187]
	v_lshlrev_b64 v[6:7], 11, v[186:187]
	v_cndmask_b32_e32 v2, v178, v179, vcc
	v_cmp_lt_i32_e32 vcc, v181, v180
	s_lshl_b32 s14, s34, 2
	v_or_b32_e32 v4, v4, v188
	v_lshl_or_b32 v6, v184, 3, v6
	v_lshlrev_b32_e32 v8, 2, v2
	v_cndmask_b32_e32 v2, v178, v181, vcc
	s_ashr_i32 s15, s14, 31
	s_waitcnt lgkmcnt(0)
	v_lshl_add_u64 v[4:5], s[20:21], 0, v[4:5]
	s_mov_b64 s[20:21], 0xc0c
	v_lshl_add_u64 v[6:7], s[22:23], 0, v[6:7]
	s_mov_b64 s[22:23], 0x400
	v_lshlrev_b32_e32 v9, 2, v2
	v_lshl_add_u64 v[2:3], v[186:187], 2, s[18:19]
	s_lshl_b64 s[18:19], s[14:15], 2
	v_lshl_add_u64 v[4:5], v[4:5], 0, s[20:21]
	s_lshl_b64 s[20:21], s[14:15], 12
	v_lshl_add_u64 v[6:7], v[6:7], 0, s[22:23]
	s_lshl_b64 s[22:23], s[14:15], 11
	s_mov_b64 s[24:25], 0
	s_mov_b32 s15, 0x42fe0000
	s_movk_i32 s28, 0x7ff
	v_mov_b32_e32 v10, v186
	v_mov_b32_e32 v12, v100
	v_mov_b32_e32 v13, v101
	v_mov_b32_e32 v14, v102
	v_mov_b32_e32 v15, v103
	v_mov_b32_e32 v16, v104
	v_mov_b32_e32 v17, v105
	v_mov_b32_e32 v18, v106
	v_mov_b32_e32 v19, v107
	v_mov_b32_e32 v20, v108
	v_mov_b32_e32 v21, v109
	v_mov_b32_e32 v22, v110
	v_mov_b32_e32 v23, v111
	v_mov_b32_e32 v24, v112
	v_mov_b32_e32 v25, v113
	v_mov_b32_e32 v26, v114
	v_mov_b32_e32 v27, v115
	s_branch .Lmy_p7a_in

; __device__ __forceinline__ float bflo(uint32_t w) { return __uint_as_float(w << 16); }
; __device__ __forceinline__ float bfhi(uint32_t w) { return __uint_as_float(w & 0xffff0000u); }
; __device__ __forceinline__ void quant_weight_rows_i8(const bf16_t* __restrict__ src, int8_t* __restrict__ dst, float* __restrict__ scl,
;                                                      int nrows, int bid, int nb) {
;     ...
;     float am = 0.f;
; #pragma unroll
;     for (int c = 0; c < 4; ++c) {
;       am = fmaxf(am, fmaxf(fmaxf(fabsf(bflo(q[c].x)), fabsf(bfhi(q[c].x))), fmaxf(fabsf(bflo(q[c].y)), fabsf(bfhi(q[c].y)))));
;       am = fmaxf(am, fmaxf(fmaxf(fabsf(bflo(q[c].z)), fabsf(bfhi(q[c].z))), fmaxf(fabsf(bflo(q[c].w)), fabsf(bfhi(q[c].w)))));
;     }
;     am = wave_max_fast(am);
;     const float inv = (am > 0.f) ? 127.f / am : 0.f;
; #pragma unroll
;     for (int c = 0; c < 4; ++c) {
;       uint2 o;
;       o.x = pack_i8x4(bflo(q[c].x) * inv, bfhi(q[c].x) * inv, bflo(q[c].y) * inv, bfhi(q[c].y) * inv);
;       o.y = pack_i8x4(bflo(q[c].z) * inv, bfhi(q[c].z) * inv, bflo(q[c].w) * inv, bfhi(q[c].w) * inv);
;       *reinterpret_cast<uint2*>(dst + (size_t)n * D + c * 512 + lane * 8) = o;
;     }
;     if (lane == 0) scl[n] = am * (1.f / 127.f);
.Lmy_p7a_in:
	s_waitcnt vmcnt(3)
	v_lshlrev_b32_e32 v29, 16, v13
	v_and_b32_e32 v13, 0xffff0000, v13
	v_lshlrev_b32_e32 v31, 16, v15
	v_and_b32_e32 v15, 0xffff0000, v15
	s_waitcnt vmcnt(2)
	v_lshlrev_b32_e32 v33, 16, v17
	v_and_b32_e32 v17, 0xffff0000, v17
	v_lshlrev_b32_e32 v35, 16, v19
	v_and_b32_e32 v19, 0xffff0000, v19
	v_max_f32_e64 v11, |v13|, |v13|
	v_max_f32_e64 v44, |v29|, |v29|
	v_max_f32_e64 v45, |v15|, |v15|
	v_max_f32_e64 v46, |v31|, |v31|
	v_lshlrev_b32_e32 v28, 16, v12
	v_and_b32_e32 v12, 0xffff0000, v12
	v_lshlrev_b32_e32 v30, 16, v14
	v_and_b32_e32 v14, 0xffff0000, v14
	s_waitcnt vmcnt(1)
	v_lshlrev_b32_e32 v37, 16, v21
	v_and_b32_e32 v21, 0xffff0000, v21
	v_lshlrev_b32_e32 v39, 16, v23
	v_and_b32_e32 v23, 0xffff0000, v23
	v_max_f32_e64 v47, |v17|, |v17|
	v_max_f32_e64 v48, |v33|, |v33|
	v_max_f32_e64 v49, |v19|, |v19|
	v_max_f32_e64 v50, |v35|, |v35|
	v_max_f32_e32 v11, v44, v11
	v_max_f32_e32 v44, v46, v45
	v_lshlrev_b32_e32 v32, 16, v16
	v_and_b32_e32 v16, 0xffff0000, v16
	v_lshlrev_b32_e32 v34, 16, v18
	v_and_b32_e32 v18, 0xffff0000, v18
	s_waitcnt vmcnt(0)
	v_lshlrev_b32_e32 v41, 16, v25
	v_and_b32_e32 v25, 0xffff0000, v25
	v_lshlrev_b32_e32 v43, 16, v27
	v_and_b32_e32 v27, 0xffff0000, v27
	v_max_f32_e64 v51, |v21|, |v21|
	v_max_f32_e64 v52, |v37|, |v37|
	v_max_f32_e64 v53, |v23|, |v23|
	v_max_f32_e64 v54, |v39|, |v39|
	v_max_f32_e32 v45, v48, v47
	v_max_f32_e32 v46, v50, v49
	v_max3_f32 v11, |v28|, |v12|, v11
	v_max3_f32 v44, |v30|, |v14|, v44
	v_lshlrev_b32_e32 v36, 16, v20
	v_and_b32_e32 v20, 0xffff0000, v20
	v_lshlrev_b32_e32 v38, 16, v22
	v_and_b32_e32 v22, 0xffff0000, v22
	v_max_f32_e64 v55, |v25|, |v25|
	v_max_f32_e64 v56, |v41|, |v41|
	v_max_f32_e64 v57, |v27|, |v27|
	v_max_f32_e64 v58, |v43|, |v43|
	v_max_f32_e32 v47, v52, v51
	v_max_f32_e32 v48, v54, v53
	v_max3_f32 v45, |v32|, |v16|, v45
	v_max3_f32 v46, |v34|, |v18|, v46
	v_max3_f32 v11, v11, 0, v44
	v_lshlrev_b32_e32 v40, 16, v24
	v_and_b32_e32 v24, 0xffff0000, v24
	v_lshlrev_b32_e32 v42, 16, v26
	v_and_b32_e32 v26, 0xffff0000, v26
	v_max_f32_e32 v49, v56, v55
	v_max_f32_e32 v50, v58, v57
	v_max3_f32 v47, |v36|, |v20|, v47
	v_max3_f32 v48, |v38|, |v22|, v48
	v_max3_f32 v11, v11, v45, v46
	v_max3_f32 v49, |v40|, |v24|, v49
	v_max3_f32 v50, |v42|, |v26|, v50
	v_max3_f32 v11, v11, v47, v48
	v_max3_f32 v11, v11, v49, v50
	s_nop 1
	v_mov_b32_dpp v44, v11 quad_perm:[1,0,3,2] row_mask:0xf bank_mask:0xf bound_ctrl:1
	v_max_f32_e32 v44, v44, v44
	v_max_f32_e32 v11, v11, v44
	s_nop 1
	v_mov_b32_dpp v44, v11 quad_perm:[2,3,0,1] row_mask:0xf bank_mask:0xf bound_ctrl:1
	v_max_f32_e32 v44, v44, v44
	v_max_f32_e32 v11, v11, v44
	s_nop 1
	v_mov_b32_dpp v44, v11 row_ror:4 row_mask:0xf bank_mask:0xf bound_ctrl:1
	v_max_f32_e32 v44, v44, v44
	v_max_f32_e32 v11, v11, v44
	s_nop 1
	v_mov_b32_dpp v44, v11 row_ror:8 row_mask:0xf bank_mask:0xf bound_ctrl:1
	v_max_f32_e32 v44, v44, v44
	v_max_f32_e32 v11, v11, v44
	ds_bpermute_b32 v44, v8, v11
	s_waitcnt lgkmcnt(0)
	v_max_f32_e32 v44, v44, v44
	v_max_f32_e32 v11, v11, v44
	ds_bpermute_b32 v44, v9, v11
	s_waitcnt lgkmcnt(0)
	v_max_f32_e32 v44, v44, v44
	v_max_f32_e32 v11, v11, v44
	v_div_scale_f32 v44, s[26:27], v11, v11, s15
	v_rcp_f32_e32 v45, v44
	v_div_scale_f32 v46, vcc, s15, v11, s15
	v_fma_f32 v47, -v44, v45, 1.0
	v_fmac_f32_e32 v45, v47, v45
	v_mul_f32_e32 v47, v46, v45
	v_fma_f32 v48, -v44, v47, v46
	v_fmac_f32_e32 v47, v48, v45
	v_fma_f32 v44, -v44, v47, v46
	v_div_fmas_f32 v44, v44, v45, v47
	v_div_fixup_f32 v44, v44, v11, s15
	v_cmp_lt_f32_e32 vcc, 0, v11
	s_nop 1
	v_cndmask_b32_e32 v44, 0, v44, vcc
	v_mul_f32_e32 v12, v44, v12
	v_mul_f32_e32 v14, v44, v14
	v_rndne_f32_e32 v12, v12
	v_rndne_f32_e32 v14, v14
	v_mul_f32_e32 v28, v44, v28
	v_mul_f32_e32 v30, v44, v30
	v_cvt_i32_f32_e32 v12, v12
	v_cvt_i32_f32_e32 v14, v14
	v_mul_f32_e32 v29, v44, v29
	v_mul_f32_e32 v13, v44, v13
	v_mul_f32_e32 v31, v44, v31
	v_mul_f32_e32 v15, v44, v15
	v_rndne_f32_e32 v28, v28
	v_rndne_f32_e32 v30, v30
	v_rndne_f32_e32 v29, v29
	v_rndne_f32_e32 v13, v13
	v_rndne_f32_e32 v31, v31
	v_rndne_f32_e32 v15, v15
	v_cvt_i32_f32_e32 v30, v30
	v_cvt_i32_f32_e32 v28, v28
	v_cvt_i32_f32_sdwa v29, v29 dst_sel:WORD_1 dst_unused:UNUSED_PAD src0_sel:DWORD
	v_cvt_i32_f32_sdwa v31, v31 dst_sel:WORD_1 dst_unused:UNUSED_PAD src0_sel:DWORD
	v_cvt_i32_f32_sdwa v13, v13 dst_sel:BYTE_3 dst_unused:UNUSED_PAD src0_sel:DWORD
	v_cvt_i32_f32_sdwa v15, v15 dst_sel:BYTE_3 dst_unused:UNUSED_PAD src0_sel:DWORD
	v_lshlrev_b32_e32 v14, 8, v14
	v_lshlrev_b32_e32 v12, 8, v12
	v_and_b32_e32 v14, 0xff00, v14
	v_and_b32_e32 v12, 0xff00, v12
	v_or_b32_sdwa v14, v30, v14 dst_sel:DWORD dst_unused:UNUSED_PAD src0_sel:BYTE_0 src1_sel:DWORD
	v_or_b32_sdwa v12, v28, v12 dst_sel:DWORD dst_unused:UNUSED_PAD src0_sel:BYTE_0 src1_sel:DWORD
	v_and_b32_e32 v31, 0xff0000, v31
	v_and_b32_e32 v29, 0xff0000, v29
	v_or_b32_e32 v14, v14, v15
	v_or_b32_e32 v12, v12, v13
	v_or_b32_e32 v13, v14, v31
	v_or_b32_e32 v12, v12, v29
	global_store_dwordx2 v[6:7], v[12:13], off offset:-1024
	v_mul_f32_e32 v13, v44, v16
	v_mul_f32_e32 v15, v44, v17
	v_mul_f32_e32 v17, v44, v18
	v_rndne_f32_e32 v13, v13
	v_rndne_f32_e32 v17, v17
	v_mul_f32_e32 v12, v44, v32
	v_mul_f32_e32 v16, v44, v34
	v_cvt_i32_f32_e32 v13, v13
	v_cvt_i32_f32_e32 v17, v17
	v_mul_f32_e32 v14, v44, v33
	v_rndne_f32_e32 v12, v12
	v_mul_f32_e32 v18, v44, v35
	v_mul_f32_e32 v19, v44, v19
	v_rndne_f32_e32 v16, v16
	v_rndne_f32_e32 v14, v14
	v_rndne_f32_e32 v15, v15
	v_rndne_f32_e32 v18, v18
	v_rndne_f32_e32 v19, v19
; __device__ __forceinline__ float bflo(uint32_t w) { return __uint_as_float(w << 16); }
; __device__ __forceinline__ float bfhi(uint32_t w) { return __uint_as_float(w & 0xffff0000u); }
; __device__ __forceinline__ void quant_weight_rows_i8(const bf16_t* __restrict__ src, int8_t* __restrict__ dst, float* __restrict__ scl,
;                                                      int nrows, int bid, int nb) {
;     ...
;     for (int c = 0; c < 4; ++c) {
;       uint2 o;
;       o.x = pack_i8x4(bflo(q[c].x) * inv, bfhi(q[c].x) * inv, bflo(q[c].y) * inv, bfhi(q[c].y) * inv);
;       o.y = pack_i8x4(bflo(q[c].z) * inv, bfhi(q[c].z) * inv, bflo(q[c].w) * inv, bfhi(q[c].w) * inv);
;       *reinterpret_cast<uint2*>(dst + (size_t)n * D + c * 512 + lane * 8) = o;
;     }
;     if (lane == 0) scl[n] = am * (1.f / 127.f);
; __device__ void phase_ssm_post(KParams& p, int bid, int nb, char* smem) {
;     ...
;   quant_weight_rows_i8(p.w_q_t, p.wq8, p.wqscale, 1024, bid, nb);
	v_cvt_i32_f32_e32 v16, v16
	v_cvt_i32_f32_e32 v12, v12
	v_cvt_i32_f32_sdwa v14, v14 dst_sel:WORD_1 dst_unused:UNUSED_PAD src0_sel:DWORD
	v_cvt_i32_f32_sdwa v18, v18 dst_sel:WORD_1 dst_unused:UNUSED_PAD src0_sel:DWORD
	v_cvt_i32_f32_sdwa v15, v15 dst_sel:BYTE_3 dst_unused:UNUSED_PAD src0_sel:DWORD
	v_cvt_i32_f32_sdwa v19, v19 dst_sel:BYTE_3 dst_unused:UNUSED_PAD src0_sel:DWORD
	v_lshlrev_b32_e32 v17, 8, v17
	v_lshlrev_b32_e32 v13, 8, v13
	v_and_b32_e32 v17, 0xff00, v17
	v_and_b32_e32 v13, 0xff00, v13
	v_or_b32_sdwa v16, v16, v17 dst_sel:DWORD dst_unused:UNUSED_PAD src0_sel:BYTE_0 src1_sel:DWORD
	v_or_b32_sdwa v12, v12, v13 dst_sel:DWORD dst_unused:UNUSED_PAD src0_sel:BYTE_0 src1_sel:DWORD
	v_and_b32_e32 v18, 0xff0000, v18
	v_and_b32_e32 v14, 0xff0000, v14
	v_or_b32_e32 v13, v16, v19
	v_or_b32_e32 v12, v12, v15
	v_or_b32_e32 v13, v13, v18
	v_or_b32_e32 v12, v12, v14
	global_store_dwordx2 v[6:7], v[12:13], off offset:-512
	v_mul_f32_e32 v13, v44, v20
	v_mul_f32_e32 v17, v44, v22
	v_rndne_f32_e32 v13, v13
	v_rndne_f32_e32 v17, v17
	v_mul_f32_e32 v12, v44, v36
	v_mul_f32_e32 v16, v44, v38
	v_cvt_i32_f32_e32 v13, v13
	v_cvt_i32_f32_e32 v17, v17
	v_mul_f32_e32 v14, v44, v37
	v_mul_f32_e32 v15, v44, v21
	v_rndne_f32_e32 v12, v12
	v_mul_f32_e32 v18, v44, v39
	v_mul_f32_e32 v19, v44, v23
	v_rndne_f32_e32 v16, v16
	v_rndne_f32_e32 v14, v14
	v_rndne_f32_e32 v15, v15
	v_rndne_f32_e32 v18, v18
	v_rndne_f32_e32 v19, v19
	v_cvt_i32_f32_e32 v16, v16
	v_cvt_i32_f32_e32 v12, v12
	v_cvt_i32_f32_sdwa v14, v14 dst_sel:WORD_1 dst_unused:UNUSED_PAD src0_sel:DWORD
	v_cvt_i32_f32_sdwa v18, v18 dst_sel:WORD_1 dst_unused:UNUSED_PAD src0_sel:DWORD
	v_cvt_i32_f32_sdwa v15, v15 dst_sel:BYTE_3 dst_unused:UNUSED_PAD src0_sel:DWORD
	v_cvt_i32_f32_sdwa v19, v19 dst_sel:BYTE_3 dst_unused:UNUSED_PAD src0_sel:DWORD
	v_lshlrev_b32_e32 v17, 8, v17
	v_lshlrev_b32_e32 v13, 8, v13
	v_and_b32_e32 v17, 0xff00, v17
	v_and_b32_e32 v13, 0xff00, v13
	v_or_b32_sdwa v16, v16, v17 dst_sel:DWORD dst_unused:UNUSED_PAD src0_sel:BYTE_0 src1_sel:DWORD
	v_or_b32_sdwa v12, v12, v13 dst_sel:DWORD dst_unused:UNUSED_PAD src0_sel:BYTE_0 src1_sel:DWORD
	v_and_b32_e32 v18, 0xff0000, v18
	v_and_b32_e32 v14, 0xff0000, v14
	v_or_b32_e32 v13, v16, v19
	v_or_b32_e32 v12, v12, v15
	v_or_b32_e32 v13, v13, v18
	v_or_b32_e32 v12, v12, v14
	global_store_dwordx2 v[6:7], v[12:13], off
	v_mul_f32_e32 v13, v44, v24
	v_mul_f32_e32 v17, v44, v26
	v_rndne_f32_e32 v13, v13
	v_rndne_f32_e32 v17, v17
	v_mul_f32_e32 v12, v44, v40
	v_mul_f32_e32 v16, v44, v42
	v_cvt_i32_f32_e32 v13, v13
	v_cvt_i32_f32_e32 v17, v17
	v_mul_f32_e32 v14, v44, v41
	v_mul_f32_e32 v15, v44, v25
	v_rndne_f32_e32 v12, v12
	v_mul_f32_e32 v18, v44, v43
	v_mul_f32_e32 v19, v44, v27
	v_rndne_f32_e32 v16, v16
	v_rndne_f32_e32 v14, v14
	v_rndne_f32_e32 v15, v15
	v_rndne_f32_e32 v18, v18
	v_rndne_f32_e32 v19, v19
	v_cvt_i32_f32_e32 v16, v16
	v_cvt_i32_f32_e32 v12, v12
	v_cvt_i32_f32_sdwa v14, v14 dst_sel:WORD_1 dst_unused:UNUSED_PAD src0_sel:DWORD
	v_cvt_i32_f32_sdwa v18, v18 dst_sel:WORD_1 dst_unused:UNUSED_PAD src0_sel:DWORD
	v_cvt_i32_f32_sdwa v15, v15 dst_sel:BYTE_3 dst_unused:UNUSED_PAD src0_sel:DWORD
	v_cvt_i32_f32_sdwa v19, v19 dst_sel:BYTE_3 dst_unused:UNUSED_PAD src0_sel:DWORD
	v_lshlrev_b32_e32 v17, 8, v17
	v_lshlrev_b32_e32 v13, 8, v13
	v_and_b32_e32 v17, 0xff00, v17
	v_and_b32_e32 v13, 0xff00, v13
	v_or_b32_sdwa v16, v16, v17 dst_sel:DWORD dst_unused:UNUSED_PAD src0_sel:BYTE_0 src1_sel:DWORD
	v_or_b32_sdwa v12, v12, v13 dst_sel:DWORD dst_unused:UNUSED_PAD src0_sel:BYTE_0 src1_sel:DWORD
	v_and_b32_e32 v18, 0xff0000, v18
	v_and_b32_e32 v14, 0xff0000, v14
	v_or_b32_e32 v13, v16, v19
	v_or_b32_e32 v12, v12, v15
	v_or_b32_e32 v13, v13, v18
	v_or_b32_e32 v12, v12, v14
	global_store_dwordx2 v[6:7], v[12:13], off offset:512
	s_and_saveexec_b64 s[26:27], s[8:9]
	s_cbranch_execz .LBB0_1007
	v_mul_f32_e32 v11, 0x3c010204, v11
	global_store_dword v[2:3], v11, off
	s_branch .LBB0_1007
.LBB0_1010:
	s_or_b64 exec, exec, s[12:13]
	s_movk_i32 s12, 0x400
	v_cmp_gt_i32_e32 vcc, s12, v186
	s_and_saveexec_b64 s[12:13], vcc
	s_cbranch_execz .LBB0_1015
	s_load_dwordx4 s[20:23], s[16:17], 0x138
	s_load_dwordx2 s[18:19], s[16:17], 0x158
	v_cmp_lt_i32_e32 vcc, v179, v180
	v_lshlrev_b64 v[6:7], 11, v[186:187]
	s_lshl_b32 s14, s34, 2
	v_cndmask_b32_e32 v4, v178, v179, vcc
	v_cmp_lt_i32_e32 vcc, v181, v180
	v_lshlrev_b32_e32 v8, 2, v4
	v_lshl_or_b32 v6, v184, 3, v6
	v_cndmask_b32_e32 v4, v178, v181, vcc
	v_lshlrev_b32_e32 v9, 2, v4
	v_lshlrev_b64 v[4:5], 12, v[186:187]
	v_or_b32_e32 v4, v4, v188
	s_waitcnt lgkmcnt(0)
	v_mov_b32_e32 v2, s22
	v_mov_b32_e32 v3, s23
	s_ashr_i32 s15, s14, 31
	v_lshl_add_u64 v[4:5], s[18:19], 0, v[4:5]
	s_mov_b64 s[18:19], 0xc0c
	v_lshl_add_u64 v[6:7], s[20:21], 0, v[6:7]
	s_mov_b64 s[20:21], 0x400
	v_lshl_add_u64 v[2:3], v[186:187], 2, v[2:3]
	s_lshl_b64 s[16:17], s[14:15], 2
	v_lshl_add_u64 v[4:5], v[4:5], 0, s[18:19]
	s_lshl_b64 s[18:19], s[14:15], 12
	v_lshl_add_u64 v[6:7], v[6:7], 0, s[20:21]
	s_lshl_b64 s[20:21], s[14:15], 11
	s_mov_b64 s[22:23], 0
	s_mov_b32 s15, 0x42fe0000
	s_movk_i32 s26, 0x3ff
	v_mov_b32_e32 v10, v186
	v_mov_b32_e32 v12, v116
	v_mov_b32_e32 v13, v117
	v_mov_b32_e32 v14, v118
	v_mov_b32_e32 v15, v119
	v_mov_b32_e32 v16, v120
	v_mov_b32_e32 v17, v121
	v_mov_b32_e32 v18, v122
	v_mov_b32_e32 v19, v123
	v_mov_b32_e32 v20, v124
	v_mov_b32_e32 v21, v125
	v_mov_b32_e32 v22, v126
	v_mov_b32_e32 v23, v127
	v_mov_b32_e32 v24, v128
	v_mov_b32_e32 v25, v129
	v_mov_b32_e32 v26, v130
	v_mov_b32_e32 v27, v131
	s_branch .Lmy_p7b_in

; __device__ __forceinline__ float bflo(uint32_t w) { return __uint_as_float(w << 16); }
; __device__ __forceinline__ float bfhi(uint32_t w) { return __uint_as_float(w & 0xffff0000u); }
; __device__ __forceinline__ void quant_weight_rows_i8(const bf16_t* __restrict__ src, int8_t* __restrict__ dst, float* __restrict__ scl,
;                                                      int nrows, int bid, int nb) {
;     ...
;     float am = 0.f;
; #pragma unroll
;     for (int c = 0; c < 4; ++c) {
;       am = fmaxf(am, fmaxf(fmaxf(fabsf(bflo(q[c].x)), fabsf(bfhi(q[c].x))), fmaxf(fabsf(bflo(q[c].y)), fabsf(bfhi(q[c].y)))));
;       am = fmaxf(am, fmaxf(fmaxf(fabsf(bflo(q[c].z)), fabsf(bfhi(q[c].z))), fmaxf(fabsf(bflo(q[c].w)), fabsf(bfhi(q[c].w)))));
;     }
;     am = wave_max_fast(am);
.Lmy_p7b_in:
	s_waitcnt vmcnt(3)
	v_lshlrev_b32_e32 v29, 16, v13
	v_and_b32_e32 v13, 0xffff0000, v13
	v_lshlrev_b32_e32 v31, 16, v15
	v_and_b32_e32 v15, 0xffff0000, v15
	s_waitcnt vmcnt(2)
	v_lshlrev_b32_e32 v33, 16, v17
	v_and_b32_e32 v17, 0xffff0000, v17
	v_lshlrev_b32_e32 v35, 16, v19
	v_and_b32_e32 v19, 0xffff0000, v19
	v_max_f32_e64 v11, |v13|, |v13|
	v_max_f32_e64 v44, |v29|, |v29|
	v_max_f32_e64 v45, |v15|, |v15|
	v_max_f32_e64 v46, |v31|, |v31|
	v_lshlrev_b32_e32 v28, 16, v12
	v_and_b32_e32 v12, 0xffff0000, v12
	v_lshlrev_b32_e32 v30, 16, v14
	v_and_b32_e32 v14, 0xffff0000, v14
	s_waitcnt vmcnt(1)
	v_lshlrev_b32_e32 v37, 16, v21
	v_and_b32_e32 v21, 0xffff0000, v21
	v_lshlrev_b32_e32 v39, 16, v23
	v_and_b32_e32 v23, 0xffff0000, v23
	v_max_f32_e64 v47, |v17|, |v17|
	v_max_f32_e64 v48, |v33|, |v33|
	v_max_f32_e64 v49, |v19|, |v19|
	v_max_f32_e64 v50, |v35|, |v35|
	v_max_f32_e32 v11, v44, v11
	v_max_f32_e32 v44, v46, v45
	v_lshlrev_b32_e32 v32, 16, v16
	v_and_b32_e32 v16, 0xffff0000, v16
	v_lshlrev_b32_e32 v34, 16, v18
	v_and_b32_e32 v18, 0xffff0000, v18
	s_waitcnt vmcnt(0)
	v_lshlrev_b32_e32 v41, 16, v25
	v_and_b32_e32 v25, 0xffff0000, v25
	v_lshlrev_b32_e32 v43, 16, v27
	v_and_b32_e32 v27, 0xffff0000, v27
	v_max_f32_e64 v51, |v21|, |v21|
	v_max_f32_e64 v52, |v37|, |v37|
	v_max_f32_e64 v53, |v23|, |v23|
	v_max_f32_e64 v54, |v39|, |v39|
	v_max_f32_e32 v45, v48, v47
	v_max_f32_e32 v46, v50, v49
	v_max3_f32 v11, |v28|, |v12|, v11
	v_max3_f32 v44, |v30|, |v14|, v44
	v_lshlrev_b32_e32 v36, 16, v20
	v_and_b32_e32 v20, 0xffff0000, v20
	v_lshlrev_b32_e32 v38, 16, v22
	v_and_b32_e32 v22, 0xffff0000, v22
	v_max_f32_e64 v55, |v25|, |v25|
	v_max_f32_e64 v56, |v41|, |v41|
	v_max_f32_e64 v57, |v27|, |v27|
	v_max_f32_e64 v58, |v43|, |v43|
	v_max_f32_e32 v47, v52, v51
	v_max_f32_e32 v48, v54, v53
	v_max3_f32 v45, |v32|, |v16|, v45
	v_max3_f32 v46, |v34|, |v18|, v46
	v_max3_f32 v11, v11, 0, v44
	v_lshlrev_b32_e32 v40, 16, v24
	v_and_b32_e32 v24, 0xffff0000, v24
	v_lshlrev_b32_e32 v42, 16, v26
	v_and_b32_e32 v26, 0xffff0000, v26
	v_max_f32_e32 v49, v56, v55
	v_max_f32_e32 v50, v58, v57
	v_max3_f32 v47, |v36|, |v20|, v47
	v_max3_f32 v48, |v38|, |v22|, v48
	v_max3_f32 v11, v11, v45, v46
	v_max3_f32 v49, |v40|, |v24|, v49
	v_max3_f32 v50, |v42|, |v26|, v50
	v_max3_f32 v11, v11, v47, v48
	v_max3_f32 v11, v11, v49, v50
	s_nop 1
	v_mov_b32_dpp v44, v11 quad_perm:[1,0,3,2] row_mask:0xf bank_mask:0xf bound_ctrl:1
	v_max_f32_e32 v44, v44, v44
	v_max_f32_e32 v11, v11, v44
	s_nop 1
	v_mov_b32_dpp v44, v11 quad_perm:[2,3,0,1] row_mask:0xf bank_mask:0xf bound_ctrl:1
	v_max_f32_e32 v44, v44, v44
	v_max_f32_e32 v11, v11, v44
	s_nop 1
	v_mov_b32_dpp v44, v11 row_ror:4 row_mask:0xf bank_mask:0xf bound_ctrl:1
	v_max_f32_e32 v44, v44, v44
	v_max_f32_e32 v11, v11, v44
	s_nop 1
	v_mov_b32_dpp v44, v11 row_ror:8 row_mask:0xf bank_mask:0xf bound_ctrl:1
	v_max_f32_e32 v44, v44, v44
	v_max_f32_e32 v11, v11, v44
	ds_bpermute_b32 v44, v8, v11
	s_waitcnt lgkmcnt(0)
	v_max_f32_e32 v44, v44, v44
	v_max_f32_e32 v11, v11, v44
	ds_bpermute_b32 v44, v9, v11
	s_waitcnt lgkmcnt(0)
; __device__ __forceinline__ float bflo(uint32_t w) { return __uint_as_float(w << 16); }
; __device__ __forceinline__ float bfhi(uint32_t w) { return __uint_as_float(w & 0xffff0000u); }
; __device__ __forceinline__ void quant_weight_rows_i8(const bf16_t* __restrict__ src, int8_t* __restrict__ dst, float* __restrict__ scl,
;                                                      int nrows, int bid, int nb) {
;     ...
;     am = wave_max_fast(am);
;     const float inv = (am > 0.f) ? 127.f / am : 0.f;
; #pragma unroll
;     for (int c = 0; c < 4; ++c) {
;       uint2 o;
;       o.x = pack_i8x4(bflo(q[c].x) * inv, bfhi(q[c].x) * inv, bflo(q[c].y) * inv, bfhi(q[c].y) * inv);
;       o.y = pack_i8x4(bflo(q[c].z) * inv, bfhi(q[c].z) * inv, bflo(q[c].w) * inv, bfhi(q[c].w) * inv);
;       *reinterpret_cast<uint2*>(dst + (size_t)n * D + c * 512 + lane * 8) = o;
;     }
;     if (lane == 0) scl[n] = am * (1.f / 127.f);
	v_max_f32_e32 v44, v44, v44
	v_max_f32_e32 v11, v11, v44
	v_div_scale_f32 v44, s[24:25], v11, v11, s15
	v_rcp_f32_e32 v45, v44
	v_div_scale_f32 v46, vcc, s15, v11, s15
	v_fma_f32 v47, -v44, v45, 1.0
	v_fmac_f32_e32 v45, v47, v45
	v_mul_f32_e32 v47, v46, v45
	v_fma_f32 v48, -v44, v47, v46
	v_fmac_f32_e32 v47, v48, v45
	v_fma_f32 v44, -v44, v47, v46
	v_div_fmas_f32 v44, v44, v45, v47
	v_div_fixup_f32 v44, v44, v11, s15
	v_cmp_lt_f32_e32 vcc, 0, v11
	s_nop 1
	v_cndmask_b32_e32 v44, 0, v44, vcc
	v_mul_f32_e32 v12, v44, v12
	v_mul_f32_e32 v14, v44, v14
	v_rndne_f32_e32 v12, v12
	v_rndne_f32_e32 v14, v14
	v_mul_f32_e32 v28, v44, v28
	v_mul_f32_e32 v30, v44, v30
	v_cvt_i32_f32_e32 v12, v12
	v_cvt_i32_f32_e32 v14, v14
	v_mul_f32_e32 v29, v44, v29
	v_mul_f32_e32 v13, v44, v13
	v_mul_f32_e32 v31, v44, v31
	v_mul_f32_e32 v15, v44, v15
	v_rndne_f32_e32 v28, v28
	v_rndne_f32_e32 v30, v30
	v_rndne_f32_e32 v29, v29
	v_rndne_f32_e32 v13, v13
	v_rndne_f32_e32 v31, v31
	v_rndne_f32_e32 v15, v15
	v_cvt_i32_f32_e32 v30, v30
	v_cvt_i32_f32_e32 v28, v28
	v_cvt_i32_f32_sdwa v29, v29 dst_sel:WORD_1 dst_unused:UNUSED_PAD src0_sel:DWORD
	v_cvt_i32_f32_sdwa v31, v31 dst_sel:WORD_1 dst_unused:UNUSED_PAD src0_sel:DWORD
	v_cvt_i32_f32_sdwa v13, v13 dst_sel:BYTE_3 dst_unused:UNUSED_PAD src0_sel:DWORD
	v_cvt_i32_f32_sdwa v15, v15 dst_sel:BYTE_3 dst_unused:UNUSED_PAD src0_sel:DWORD
	v_lshlrev_b32_e32 v14, 8, v14
	v_lshlrev_b32_e32 v12, 8, v12
	v_and_b32_e32 v14, 0xff00, v14
	v_and_b32_e32 v12, 0xff00, v12
	v_or_b32_sdwa v14, v30, v14 dst_sel:DWORD dst_unused:UNUSED_PAD src0_sel:BYTE_0 src1_sel:DWORD
	v_or_b32_sdwa v12, v28, v12 dst_sel:DWORD dst_unused:UNUSED_PAD src0_sel:BYTE_0 src1_sel:DWORD
	v_and_b32_e32 v31, 0xff0000, v31
	v_and_b32_e32 v29, 0xff0000, v29
	v_or_b32_e32 v14, v14, v15
	v_or_b32_e32 v12, v12, v13
	v_or_b32_e32 v13, v14, v31
	v_or_b32_e32 v12, v12, v29
	global_store_dwordx2 v[6:7], v[12:13], off offset:-1024
	v_mul_f32_e32 v13, v44, v16
	v_mul_f32_e32 v15, v44, v17
	v_mul_f32_e32 v17, v44, v18
	v_rndne_f32_e32 v13, v13
	v_rndne_f32_e32 v17, v17
	v_mul_f32_e32 v12, v44, v32
	v_mul_f32_e32 v16, v44, v34
	v_cvt_i32_f32_e32 v13, v13
	v_cvt_i32_f32_e32 v17, v17
	v_mul_f32_e32 v14, v44, v33
	v_rndne_f32_e32 v12, v12
	v_mul_f32_e32 v18, v44, v35
	v_mul_f32_e32 v19, v44, v19
	v_rndne_f32_e32 v16, v16
	v_rndne_f32_e32 v14, v14
	v_rndne_f32_e32 v15, v15
	v_rndne_f32_e32 v18, v18
	v_rndne_f32_e32 v19, v19
	v_cvt_i32_f32_e32 v16, v16
	v_cvt_i32_f32_e32 v12, v12
	v_cvt_i32_f32_sdwa v14, v14 dst_sel:WORD_1 dst_unused:UNUSED_PAD src0_sel:DWORD
	v_cvt_i32_f32_sdwa v18, v18 dst_sel:WORD_1 dst_unused:UNUSED_PAD src0_sel:DWORD
	v_cvt_i32_f32_sdwa v15, v15 dst_sel:BYTE_3 dst_unused:UNUSED_PAD src0_sel:DWORD
	v_cvt_i32_f32_sdwa v19, v19 dst_sel:BYTE_3 dst_unused:UNUSED_PAD src0_sel:DWORD
	v_lshlrev_b32_e32 v17, 8, v17
	v_lshlrev_b32_e32 v13, 8, v13
	v_and_b32_e32 v17, 0xff00, v17
	v_and_b32_e32 v13, 0xff00, v13
	v_or_b32_sdwa v16, v16, v17 dst_sel:DWORD dst_unused:UNUSED_PAD src0_sel:BYTE_0 src1_sel:DWORD
	v_or_b32_sdwa v12, v12, v13 dst_sel:DWORD dst_unused:UNUSED_PAD src0_sel:BYTE_0 src1_sel:DWORD
	v_and_b32_e32 v18, 0xff0000, v18
	v_and_b32_e32 v14, 0xff0000, v14
	v_or_b32_e32 v13, v16, v19
	v_or_b32_e32 v12, v12, v15
	v_or_b32_e32 v13, v13, v18
	v_or_b32_e32 v12, v12, v14
	global_store_dwordx2 v[6:7], v[12:13], off offset:-512
	v_mul_f32_e32 v13, v44, v20
	v_mul_f32_e32 v17, v44, v22
	v_rndne_f32_e32 v13, v13
	v_rndne_f32_e32 v17, v17
	v_mul_f32_e32 v12, v44, v36
	v_mul_f32_e32 v16, v44, v38
	v_cvt_i32_f32_e32 v13, v13
	v_cvt_i32_f32_e32 v17, v17
	v_mul_f32_e32 v14, v44, v37
	v_mul_f32_e32 v15, v44, v21
	v_rndne_f32_e32 v12, v12
	v_mul_f32_e32 v18, v44, v39
	v_mul_f32_e32 v19, v44, v23
	v_rndne_f32_e32 v16, v16
	v_rndne_f32_e32 v14, v14
	v_rndne_f32_e32 v15, v15
	v_rndne_f32_e32 v18, v18
	v_rndne_f32_e32 v19, v19
	v_cvt_i32_f32_e32 v16, v16
	v_cvt_i32_f32_e32 v12, v12
	v_cvt_i32_f32_sdwa v14, v14 dst_sel:WORD_1 dst_unused:UNUSED_PAD src0_sel:DWORD
	v_cvt_i32_f32_sdwa v18, v18 dst_sel:WORD_1 dst_unused:UNUSED_PAD src0_sel:DWORD
	v_cvt_i32_f32_sdwa v15, v15 dst_sel:BYTE_3 dst_unused:UNUSED_PAD src0_sel:DWORD
	v_cvt_i32_f32_sdwa v19, v19 dst_sel:BYTE_3 dst_unused:UNUSED_PAD src0_sel:DWORD
	v_lshlrev_b32_e32 v17, 8, v17
	v_lshlrev_b32_e32 v13, 8, v13
	v_and_b32_e32 v17, 0xff00, v17
	v_and_b32_e32 v13, 0xff00, v13
	v_or_b32_sdwa v16, v16, v17 dst_sel:DWORD dst_unused:UNUSED_PAD src0_sel:BYTE_0 src1_sel:DWORD
	v_or_b32_sdwa v12, v12, v13 dst_sel:DWORD dst_unused:UNUSED_PAD src0_sel:BYTE_0 src1_sel:DWORD
	v_and_b32_e32 v18, 0xff0000, v18
	v_and_b32_e32 v14, 0xff0000, v14
	v_or_b32_e32 v13, v16, v19
	v_or_b32_e32 v12, v12, v15
	v_or_b32_e32 v13, v13, v18
	v_or_b32_e32 v12, v12, v14
	global_store_dwordx2 v[6:7], v[12:13], off
	v_mul_f32_e32 v13, v44, v24
	v_mul_f32_e32 v17, v44, v26
	v_rndne_f32_e32 v13, v13
	v_rndne_f32_e32 v17, v17
	v_mul_f32_e32 v12, v44, v40
	v_mul_f32_e32 v16, v44, v42
	v_cvt_i32_f32_e32 v13, v13
	v_cvt_i32_f32_e32 v17, v17
	v_mul_f32_e32 v14, v44, v41
	v_mul_f32_e32 v15, v44, v25
	v_rndne_f32_e32 v12, v12
	v_mul_f32_e32 v18, v44, v43
	v_mul_f32_e32 v19, v44, v27
	v_rndne_f32_e32 v16, v16
	v_rndne_f32_e32 v14, v14
	v_rndne_f32_e32 v15, v15
	v_rndne_f32_e32 v18, v18
	v_rndne_f32_e32 v19, v19
	v_cvt_i32_f32_e32 v16, v16
	v_cvt_i32_f32_e32 v12, v12
	v_cvt_i32_f32_sdwa v14, v14 dst_sel:WORD_1 dst_unused:UNUSED_PAD src0_sel:DWORD
	v_cvt_i32_f32_sdwa v18, v18 dst_sel:WORD_1 dst_unused:UNUSED_PAD src0_sel:DWORD
	v_cvt_i32_f32_sdwa v15, v15 dst_sel:BYTE_3 dst_unused:UNUSED_PAD src0_sel:DWORD
	v_cvt_i32_f32_sdwa v19, v19 dst_sel:BYTE_3 dst_unused:UNUSED_PAD src0_sel:DWORD
	v_lshlrev_b32_e32 v17, 8, v17
	v_lshlrev_b32_e32 v13, 8, v13
	v_and_b32_e32 v17, 0xff00, v17
	v_and_b32_e32 v13, 0xff00, v13
	v_or_b32_sdwa v16, v16, v17 dst_sel:DWORD dst_unused:UNUSED_PAD src0_sel:BYTE_0 src1_sel:DWORD
	v_or_b32_sdwa v12, v12, v13 dst_sel:DWORD dst_unused:UNUSED_PAD src0_sel:BYTE_0 src1_sel:DWORD
	v_and_b32_e32 v18, 0xff0000, v18
	v_and_b32_e32 v14, 0xff0000, v14
	v_or_b32_e32 v13, v16, v19
	v_or_b32_e32 v12, v12, v15
	v_or_b32_e32 v13, v13, v18
	v_or_b32_e32 v12, v12, v14
	global_store_dwordx2 v[6:7], v[12:13], off offset:512
	s_and_saveexec_b64 s[24:25], s[8:9]
	s_cbranch_execz .LBB0_1012
	v_mul_f32_e32 v11, 0x3c010204, v11
	global_store_dword v[2:3], v11, off
	s_branch .LBB0_1012
